# E: oproj residual epilogue: the 16 per-lane X-row read-modify-write loads are issued up front (10 in flight, slots reused) with counted vmcnt instead of load/vmcnt(0)/store per piece
# speedup vs baseline: 1.0043x; 1.0043x over previous
; __device__ __forceinline__ unsigned cvt_pk_bf16(float lo, float hi) { unsigned r; asm volatile("v_cvt_pk_bf16_f32 %0, %1, %2" : "=v"(r) : "v"(lo), "v"(hi)); return r; }
;     __device__ __forceinline__ void operator()(const pg8::f32x4 (&acc)[2][2][4][2], const pg8::Unit& u, int wr, int wc, int fr, int fq) const {
;     ...
;             for (int m = 0; m < 4; ++m) { const size_t row = (size_t)(u.pm * 256 + rowoff + ai * 128 + wr * 64 + m * 16 + fr); bf16_t* rowp = X + row * 1024 + col0; float sq = 0.f;
; #pragma unroll
;                 for (int bj = 0; bj < 2; ++bj) { pg8::u32x4* ptr = (pg8::u32x4*)(rowp + bj * 128); const pg8::u32x4 xo = *ptr;
;                     const f32x4 v0 = gv[bj][0] * (acc[ai][bj][m][0] + bv[bj][0]), v1 = gv[bj][1] * (acc[ai][bj][m][1] + bv[bj][1]);
;                     pg8::u32x4 w;
;                     w.x = pg8::cvt_pk_bf16(bf2f(xo.x & 0xffffu) + v0[0], bf2f(xo.x >> 16) + v0[1]); w.y = pg8::cvt_pk_bf16(bf2f(xo.y & 0xffffu) + v0[2], bf2f(xo.y >> 16) + v0[3]);
;                     w.z = pg8::cvt_pk_bf16(bf2f(xo.z & 0xffffu) + v1[0], bf2f(xo.z >> 16) + v1[1]); w.w = pg8::cvt_pk_bf16(bf2f(xo.w & 0xffffu) + v1[2], bf2f(xo.w >> 16) + v1[3]);
;                     *ptr = w;
;                     { const float r0 = bf2f(w.x & 0xffffu), r1 = bf2f(w.x >> 16), r2 = bf2f(w.y & 0xffffu), r3 = bf2f(w.y >> 16), r4 = bf2f(w.z & 0xffffu), r5 = bf2f(w.z >> 16), r6 = bf2f(w.w & 0xffffu), r7 = bf2f(w.w >> 16);
;                       sq += (r0 * r0 + r1 * r1) + (r2 * r2 + r3 * r3) + (r4 * r4 + r5 * r5) + (r6 * r6 + r7 * r7); } }
;                 sq += __shfl_xor(sq, 16); sq += __shfl_xor(sq, 32);
;                 if (fq == 0) ssq[row * 16 + u.pn * 4 + wc] = sq; }
.LBB0_1187:
	s_lshl_b32 s14, s14, 8
	v_add_u32_e32 v176, s14, v1
	v_ashrrev_i32_e32 v177, 31, v176
	v_readlane_b32 s4, v250, 6
	v_lshlrev_b64 v[178:179], 11, v[176:177]
	v_readlane_b32 s5, v250, 7
	global_load_dwordx4 v[56:59], v[58:59], off offset:528
	s_waitcnt vmcnt(0)
	v_pk_add_f32 v[160:161], v[160:161], v[52:53]
	v_lshl_add_u64 v[178:179], s[4:5], 0, v[178:179]
	v_lshl_add_u64 v[178:179], v[174:175], 1, v[178:179]
	v_mov_b32_e32 v204, v178
	v_mov_b32_e32 v205, v179
	global_load_dwordx4 v[192:195], v[178:179], off
	global_load_dwordx4 v[196:199], v[178:179], off offset:256
	s_mov_b64 s[20:21], 0x8000
	v_lshl_add_u64 v[220:221], v[178:179], 0, s[20:21]
	global_load_dwordx4 v[200:203], v[220:221], off
	global_load_dwordx4 v[208:211], v[220:221], off offset:256
	v_lshl_add_u64 v[220:221], v[220:221], 0, s[20:21]
	global_load_dwordx4 v[224:227], v[220:221], off
	global_load_dwordx4 v[228:231], v[220:221], off offset:256
	v_lshl_add_u64 v[220:221], v[220:221], 0, s[20:21]
	global_load_dwordx4 v[232:235], v[220:221], off
	global_load_dwordx4 v[236:239], v[220:221], off offset:256
	s_mov_b64 s[20:21], 0x40000
	v_lshl_add_u64 v[220:221], v[178:179], 0, s[20:21]
	global_load_dwordx4 v[216:219], v[220:221], off
	global_load_dwordx4 v[244:247], v[220:221], off offset:256
	v_pk_add_f32 v[158:159], v[158:159], v[46:47]
	v_pk_add_f32 v[156:157], v[156:157], v[44:45]
	v_pk_mul_f32 v[160:161], v[60:61], v[160:161]
	v_pk_mul_f32 v[190:191], v[66:67], v[158:159]
	v_pk_mul_f32 v[158:159], v[64:65], v[156:157]
	v_pk_add_f32 v[162:163], v[162:163], v[54:55]
	v_pk_add_f32 v[152:153], v[152:153], v[40:41]
	v_pk_mul_f32 v[162:163], v[62:63], v[162:163]
	v_pk_add_f32 v[150:151], v[150:151], v[38:39]
	v_pk_add_f32 v[148:149], v[148:149], v[36:37]
	v_pk_mul_f32 v[152:153], v[48:49], v[152:153]
	v_pk_add_f32 v[154:155], v[154:155], v[42:43]
	s_waitcnt vmcnt(9)
	v_lshlrev_b32_e32 v156, 16, v192
	v_and_b32_e32 v157, 0xffff0000, v192
	v_add_f32_e32 v156, v160, v156
	v_add_f32_e32 v157, v161, v157
	v_cvt_pk_bf16_f32 v156, v156, v157
	v_lshlrev_b32_e32 v157, 16, v193
	v_and_b32_e32 v160, 0xffff0000, v193
	v_add_f32_e32 v157, v162, v157
	v_add_f32_e32 v160, v163, v160
	v_cvt_pk_bf16_f32 v157, v157, v160
	v_lshlrev_b32_e32 v160, 16, v194
	v_add_f32_e32 v158, v158, v160
	v_and_b32_e32 v160, 0xffff0000, v194
	v_add_f32_e32 v159, v159, v160
	v_cvt_pk_bf16_f32 v158, v158, v159
	v_lshlrev_b32_e32 v159, 16, v195
	v_and_b32_e32 v160, 0xffff0000, v195
	v_add_f32_e32 v159, v190, v159
	v_add_f32_e32 v160, v191, v160
	v_cvt_pk_bf16_f32 v159, v159, v160
	global_store_dwordx4 v[178:179], v[156:159], off
	v_lshlrev_b32_e32 v160, 16, v156
	v_lshlrev_b32_e32 v161, 16, v157
	v_and_b32_e32 v156, 0xffff0000, v156
	v_and_b32_e32 v157, 0xffff0000, v157
	v_mul_f32_e32 v156, v156, v156
	v_mul_f32_e32 v157, v157, v157
	v_lshlrev_b32_e32 v162, 16, v158
	v_and_b32_e32 v158, 0xffff0000, v158
	v_fmac_f32_e32 v156, v160, v160
	v_fmac_f32_e32 v157, v161, v161
	v_add_f32_e32 v156, v156, v157
	v_mul_f32_e32 v157, v158, v158
	v_lshlrev_b32_e32 v163, 16, v159
	v_and_b32_e32 v159, 0xffff0000, v159
	v_fmac_f32_e32 v157, v162, v162
	v_add_f32_e32 v156, v156, v157
	v_mul_f32_e32 v157, v159, v159
	v_fmac_f32_e32 v157, v163, v163
	v_add_f32_e32 v162, v156, v157
	v_pk_mul_f32 v[160:161], v[58:59], v[150:151]
	v_pk_mul_f32 v[150:151], v[56:57], v[148:149]
	v_pk_mul_f32 v[154:155], v[50:51], v[154:155]
	s_waitcnt vmcnt(8)
	v_lshlrev_b32_e32 v148, 16, v196
	v_and_b32_e32 v149, 0xffff0000, v196
	v_add_f32_e32 v148, v152, v148
	v_add_f32_e32 v149, v153, v149
	v_cvt_pk_bf16_f32 v148, v148, v149
	v_lshlrev_b32_e32 v149, 16, v197
	v_and_b32_e32 v152, 0xffff0000, v197
	v_add_f32_e32 v149, v154, v149
	v_add_f32_e32 v152, v155, v152
	v_cvt_pk_bf16_f32 v149, v149, v152
	v_lshlrev_b32_e32 v152, 16, v198
	v_add_f32_e32 v150, v150, v152
	v_and_b32_e32 v152, 0xffff0000, v198
	v_add_f32_e32 v151, v151, v152
	v_cvt_pk_bf16_f32 v150, v150, v151
	v_lshlrev_b32_e32 v151, 16, v199
	v_and_b32_e32 v152, 0xffff0000, v199
	v_add_f32_e32 v151, v160, v151
	v_add_f32_e32 v152, v161, v152
	v_cvt_pk_bf16_f32 v151, v151, v152
	global_store_dwordx4 v[178:179], v[148:151], off offset:256
	s_mov_b64 s[20:21], 0x48000
	v_lshl_add_u64 v[220:221], v[204:205], 0, s[20:21]
	global_load_dwordx4 v[192:195], v[220:221], off
	global_load_dwordx4 v[196:199], v[220:221], off offset:256
	v_lshlrev_b32_e32 v152, 16, v148
	v_lshlrev_b32_e32 v153, 16, v149
	v_and_b32_e32 v148, 0xffff0000, v148
	v_and_b32_e32 v149, 0xffff0000, v149
	v_mul_f32_e32 v148, v148, v148
	v_mul_f32_e32 v149, v149, v149
	v_lshlrev_b32_e32 v154, 16, v150
	v_and_b32_e32 v150, 0xffff0000, v150
	v_fmac_f32_e32 v148, v152, v152
	v_fmac_f32_e32 v149, v153, v153
	v_add_f32_e32 v148, v148, v149
	v_mul_f32_e32 v149, v150, v150
	v_lshlrev_b32_e32 v155, 16, v151
	v_and_b32_e32 v151, 0xffff0000, v151
	v_fmac_f32_e32 v149, v154, v154
	v_add_f32_e32 v148, v148, v149
	v_mul_f32_e32 v149, v151, v151
	v_fmac_f32_e32 v149, v155, v155
	v_and_b32_e32 v150, 64, v207
	v_add_f32_e32 v148, v148, v149
	v_xor_b32_e32 v149, 16, v207
	v_add_u32_e32 v150, 64, v150
	v_cmp_lt_i32_e32 vcc, v149, v150
	v_add_f32_e32 v148, v162, v148
	s_nop 0
	v_cndmask_b32_e32 v149, v207, v149, vcc
	v_lshlrev_b32_e32 v152, 2, v149
	ds_bpermute_b32 v149, v152, v148
	s_waitcnt lgkmcnt(0)
	v_add_f32_e32 v148, v148, v149
	v_xor_b32_e32 v149, 32, v207
	v_cmp_lt_i32_e32 vcc, v149, v150
	s_nop 1
	v_cndmask_b32_e32 v149, v207, v149, vcc
	v_lshlrev_b32_e32 v153, 2, v149
	ds_bpermute_b32 v149, v153, v148
	s_and_saveexec_b64 s[4:5], s[42:43]
	s_cbranch_execz .LBB0_1189
	v_readlane_b32 s24, v253, 54
	s_waitcnt lgkmcnt(0)
	v_add_f32_e32 v150, v148, v149
	s_lshl_b32 s20, s87, 2
	v_lshlrev_b64 v[148:149], 6, v[176:177]
	v_readlane_b32 s25, v253, 55
	s_ashr_i32 s21, s20, 31
	s_lshl_b32 s30, s82, 2
	v_lshl_add_u64 v[148:149], s[24:25], 0, v[148:149]
	v_lshl_add_u64 v[148:149], s[20:21], 2, v[148:149]
	v_lshl_add_u64 v[148:149], v[148:149], 0, s[30:31]
	global_store_dword v[148:149], v150, off
; __device__ __forceinline__ unsigned cvt_pk_bf16(float lo, float hi) { unsigned r; asm volatile("v_cvt_pk_bf16_f32 %0, %1, %2" : "=v"(r) : "v"(lo), "v"(hi)); return r; }
;     __device__ __forceinline__ void operator()(const pg8::f32x4 (&acc)[2][2][4][2], const pg8::Unit& u, int wr, int wc, int fr, int fq) const {
;     ...
;             for (int m = 0; m < 4; ++m) { const size_t row = (size_t)(u.pm * 256 + rowoff + ai * 128 + wr * 64 + m * 16 + fr); bf16_t* rowp = X + row * 1024 + col0; float sq = 0.f;
; #pragma unroll
;                 for (int bj = 0; bj < 2; ++bj) { pg8::u32x4* ptr = (pg8::u32x4*)(rowp + bj * 128); const pg8::u32x4 xo = *ptr;
;                     const f32x4 v0 = gv[bj][0] * (acc[ai][bj][m][0] + bv[bj][0]), v1 = gv[bj][1] * (acc[ai][bj][m][1] + bv[bj][1]);
;                     pg8::u32x4 w;
;                     w.x = pg8::cvt_pk_bf16(bf2f(xo.x & 0xffffu) + v0[0], bf2f(xo.x >> 16) + v0[1]); w.y = pg8::cvt_pk_bf16(bf2f(xo.y & 0xffffu) + v0[2], bf2f(xo.y >> 16) + v0[3]);
;                     w.z = pg8::cvt_pk_bf16(bf2f(xo.z & 0xffffu) + v1[0], bf2f(xo.z >> 16) + v1[1]); w.w = pg8::cvt_pk_bf16(bf2f(xo.w & 0xffffu) + v1[2], bf2f(xo.w >> 16) + v1[3]);
;                     *ptr = w;
;                     { const float r0 = bf2f(w.x & 0xffffu), r1 = bf2f(w.x >> 16), r2 = bf2f(w.y & 0xffffu), r3 = bf2f(w.y >> 16), r4 = bf2f(w.z & 0xffffu), r5 = bf2f(w.z >> 16), r6 = bf2f(w.w & 0xffffu), r7 = bf2f(w.w >> 16);
;                       sq += (r0 * r0 + r1 * r1) + (r2 * r2 + r3 * r3) + (r4 * r4 + r5 * r5) + (r6 * r6 + r7 * r7); } }
;                 sq += __shfl_xor(sq, 16); sq += __shfl_xor(sq, 32);
;                 if (fq == 0) ssq[row * 16 + u.pn * 4 + wc] = sq; }
.LBB0_1189:
	s_or_b64 exec, exec, s[4:5]
	v_add_u32_e32 v148, s14, v182
	s_waitcnt lgkmcnt(0)
	v_ashrrev_i32_e32 v149, 31, v148
	v_readlane_b32 s4, v250, 6
	v_lshlrev_b64 v[150:151], 11, v[148:149]
	v_readlane_b32 s5, v250, 7
	v_pk_add_f32 v[144:145], v[144:145], v[52:53]
	v_pk_add_f32 v[142:143], v[142:143], v[46:47]
	v_lshl_add_u64 v[150:151], s[4:5], 0, v[150:151]
	v_lshl_add_u64 v[150:151], v[174:175], 1, v[150:151]
	v_pk_add_f32 v[140:141], v[140:141], v[44:45]
	v_pk_mul_f32 v[144:145], v[60:61], v[144:145]
	v_pk_mul_f32 v[158:159], v[66:67], v[142:143]
	v_pk_mul_f32 v[142:143], v[64:65], v[140:141]
	v_pk_add_f32 v[146:147], v[146:147], v[54:55]
	v_pk_add_f32 v[136:137], v[136:137], v[40:41]
	v_pk_mul_f32 v[146:147], v[62:63], v[146:147]
	v_pk_add_f32 v[134:135], v[134:135], v[38:39]
	v_pk_add_f32 v[132:133], v[132:133], v[36:37]
	v_pk_mul_f32 v[136:137], v[48:49], v[136:137]
	v_pk_add_f32 v[138:139], v[138:139], v[42:43]
	s_waitcnt vmcnt(9)
	v_lshlrev_b32_e32 v140, 16, v200
	v_and_b32_e32 v141, 0xffff0000, v200
	v_add_f32_e32 v140, v144, v140
	v_add_f32_e32 v141, v145, v141
	v_cvt_pk_bf16_f32 v140, v140, v141
	v_lshlrev_b32_e32 v141, 16, v201
	v_and_b32_e32 v144, 0xffff0000, v201
	v_add_f32_e32 v141, v146, v141
	v_add_f32_e32 v144, v147, v144
	v_cvt_pk_bf16_f32 v141, v141, v144
	v_lshlrev_b32_e32 v144, 16, v202
	v_add_f32_e32 v142, v142, v144
	v_and_b32_e32 v144, 0xffff0000, v202
	v_add_f32_e32 v143, v143, v144
	v_cvt_pk_bf16_f32 v142, v142, v143
	v_lshlrev_b32_e32 v143, 16, v203
	v_and_b32_e32 v144, 0xffff0000, v203
	v_add_f32_e32 v143, v158, v143
	v_add_f32_e32 v144, v159, v144
	v_cvt_pk_bf16_f32 v143, v143, v144
	global_store_dwordx4 v[150:151], v[140:143], off
	v_lshlrev_b32_e32 v144, 16, v140
	v_lshlrev_b32_e32 v145, 16, v141
	v_and_b32_e32 v140, 0xffff0000, v140
	v_and_b32_e32 v141, 0xffff0000, v141
	v_mul_f32_e32 v140, v140, v140
	v_mul_f32_e32 v141, v141, v141
	v_lshlrev_b32_e32 v146, 16, v142
	v_and_b32_e32 v142, 0xffff0000, v142
	v_fmac_f32_e32 v140, v144, v144
	v_fmac_f32_e32 v141, v145, v145
	v_add_f32_e32 v140, v140, v141
	v_mul_f32_e32 v141, v142, v142
	v_lshlrev_b32_e32 v147, 16, v143
	v_and_b32_e32 v143, 0xffff0000, v143
	v_fmac_f32_e32 v141, v146, v146
	v_add_f32_e32 v140, v140, v141
	v_mul_f32_e32 v141, v143, v143
	v_fmac_f32_e32 v141, v147, v147
	v_add_f32_e32 v146, v140, v141
	v_pk_mul_f32 v[144:145], v[58:59], v[134:135]
	v_pk_mul_f32 v[134:135], v[56:57], v[132:133]
	v_pk_mul_f32 v[138:139], v[50:51], v[138:139]
	s_waitcnt vmcnt(8)
	v_lshlrev_b32_e32 v132, 16, v208
	v_and_b32_e32 v133, 0xffff0000, v208
	v_add_f32_e32 v132, v136, v132
	v_add_f32_e32 v133, v137, v133
	v_cvt_pk_bf16_f32 v132, v132, v133
	v_lshlrev_b32_e32 v133, 16, v209
	v_and_b32_e32 v136, 0xffff0000, v209
	v_add_f32_e32 v133, v138, v133
	v_add_f32_e32 v136, v139, v136
	v_cvt_pk_bf16_f32 v133, v133, v136
	v_lshlrev_b32_e32 v136, 16, v210
	v_add_f32_e32 v134, v134, v136
	v_and_b32_e32 v136, 0xffff0000, v210
	v_add_f32_e32 v135, v135, v136
	v_cvt_pk_bf16_f32 v134, v134, v135
	v_lshlrev_b32_e32 v135, 16, v211
	v_and_b32_e32 v136, 0xffff0000, v211
	v_add_f32_e32 v135, v144, v135
	v_add_f32_e32 v136, v145, v136
	v_cvt_pk_bf16_f32 v135, v135, v136
	global_store_dwordx4 v[150:151], v[132:135], off offset:256
	s_mov_b64 s[20:21], 0x50000
	v_lshl_add_u64 v[220:221], v[204:205], 0, s[20:21]
	global_load_dwordx4 v[200:203], v[220:221], off
	global_load_dwordx4 v[208:211], v[220:221], off offset:256
	v_lshlrev_b32_e32 v136, 16, v132
	v_lshlrev_b32_e32 v137, 16, v133
	v_and_b32_e32 v132, 0xffff0000, v132
	v_and_b32_e32 v133, 0xffff0000, v133
	v_mul_f32_e32 v132, v132, v132
	v_mul_f32_e32 v133, v133, v133
	v_lshlrev_b32_e32 v138, 16, v134
	v_and_b32_e32 v134, 0xffff0000, v134
	v_fmac_f32_e32 v132, v136, v136
	v_fmac_f32_e32 v133, v137, v137
	v_add_f32_e32 v132, v132, v133
	v_mul_f32_e32 v133, v134, v134
	v_lshlrev_b32_e32 v139, 16, v135
	v_and_b32_e32 v135, 0xffff0000, v135
	v_fmac_f32_e32 v133, v138, v138
	v_add_f32_e32 v132, v132, v133
	v_mul_f32_e32 v133, v135, v135
	v_fmac_f32_e32 v133, v139, v139
	v_add_f32_e32 v132, v132, v133
	v_add_f32_e32 v132, v146, v132
	ds_bpermute_b32 v133, v152, v132
	s_waitcnt lgkmcnt(0)
	v_add_f32_e32 v132, v132, v133
	ds_bpermute_b32 v133, v153, v132
	s_and_saveexec_b64 s[4:5], s[42:43]
	s_cbranch_execz .LBB0_1191
	v_readlane_b32 s24, v253, 54
	s_waitcnt lgkmcnt(0)
	v_add_f32_e32 v134, v132, v133
	s_lshl_b32 s20, s87, 2
	v_lshlrev_b64 v[132:133], 6, v[148:149]
	v_readlane_b32 s25, v253, 55
	s_ashr_i32 s21, s20, 31
	s_lshl_b32 s30, s82, 2
	v_lshl_add_u64 v[132:133], s[24:25], 0, v[132:133]
	v_lshl_add_u64 v[132:133], s[20:21], 2, v[132:133]
	v_lshl_add_u64 v[132:133], v[132:133], 0, s[30:31]
	global_store_dword v[132:133], v134, off
; __device__ __forceinline__ unsigned cvt_pk_bf16(float lo, float hi) { unsigned r; asm volatile("v_cvt_pk_bf16_f32 %0, %1, %2" : "=v"(r) : "v"(lo), "v"(hi)); return r; }
;     __device__ __forceinline__ void operator()(const pg8::f32x4 (&acc)[2][2][4][2], const pg8::Unit& u, int wr, int wc, int fr, int fq) const {
;     ...
;             for (int m = 0; m < 4; ++m) { const size_t row = (size_t)(u.pm * 256 + rowoff + ai * 128 + wr * 64 + m * 16 + fr); bf16_t* rowp = X + row * 1024 + col0; float sq = 0.f;
; #pragma unroll
;                 for (int bj = 0; bj < 2; ++bj) { pg8::u32x4* ptr = (pg8::u32x4*)(rowp + bj * 128); const pg8::u32x4 xo = *ptr;
;                     const f32x4 v0 = gv[bj][0] * (acc[ai][bj][m][0] + bv[bj][0]), v1 = gv[bj][1] * (acc[ai][bj][m][1] + bv[bj][1]);
;                     pg8::u32x4 w;
;                     w.x = pg8::cvt_pk_bf16(bf2f(xo.x & 0xffffu) + v0[0], bf2f(xo.x >> 16) + v0[1]); w.y = pg8::cvt_pk_bf16(bf2f(xo.y & 0xffffu) + v0[2], bf2f(xo.y >> 16) + v0[3]);
;                     w.z = pg8::cvt_pk_bf16(bf2f(xo.z & 0xffffu) + v1[0], bf2f(xo.z >> 16) + v1[1]); w.w = pg8::cvt_pk_bf16(bf2f(xo.w & 0xffffu) + v1[2], bf2f(xo.w >> 16) + v1[3]);
;                     *ptr = w;
;                     { const float r0 = bf2f(w.x & 0xffffu), r1 = bf2f(w.x >> 16), r2 = bf2f(w.y & 0xffffu), r3 = bf2f(w.y >> 16), r4 = bf2f(w.z & 0xffffu), r5 = bf2f(w.z >> 16), r6 = bf2f(w.w & 0xffffu), r7 = bf2f(w.w >> 16);
;                       sq += (r0 * r0 + r1 * r1) + (r2 * r2 + r3 * r3) + (r4 * r4 + r5 * r5) + (r6 * r6 + r7 * r7); } }
;                 sq += __shfl_xor(sq, 16); sq += __shfl_xor(sq, 32);
;                 if (fq == 0) ssq[row * 16 + u.pn * 4 + wc] = sq; }
.LBB0_1191:
	s_or_b64 exec, exec, s[4:5]
	v_add_u32_e32 v132, s14, v183
	s_waitcnt lgkmcnt(0)
	v_ashrrev_i32_e32 v133, 31, v132
	v_readlane_b32 s4, v250, 6
	v_lshlrev_b64 v[134:135], 11, v[132:133]
	v_readlane_b32 s5, v250, 7
	v_pk_add_f32 v[128:129], v[128:129], v[52:53]
	v_pk_add_f32 v[126:127], v[126:127], v[46:47]
	v_lshl_add_u64 v[134:135], s[4:5], 0, v[134:135]
	v_lshl_add_u64 v[134:135], v[174:175], 1, v[134:135]
	v_pk_add_f32 v[124:125], v[124:125], v[44:45]
	v_pk_mul_f32 v[128:129], v[60:61], v[128:129]
	v_pk_mul_f32 v[140:141], v[66:67], v[126:127]
	v_pk_mul_f32 v[126:127], v[64:65], v[124:125]
	v_pk_add_f32 v[130:131], v[130:131], v[54:55]
	v_pk_add_f32 v[120:121], v[120:121], v[40:41]
	v_pk_mul_f32 v[130:131], v[62:63], v[130:131]
	v_pk_add_f32 v[118:119], v[118:119], v[38:39]
	v_pk_add_f32 v[116:117], v[116:117], v[36:37]
	v_pk_mul_f32 v[120:121], v[48:49], v[120:121]
	v_pk_add_f32 v[122:123], v[122:123], v[42:43]
	s_waitcnt vmcnt(9)
	v_lshlrev_b32_e32 v124, 16, v224
	v_and_b32_e32 v125, 0xffff0000, v224
	v_add_f32_e32 v124, v128, v124
	v_add_f32_e32 v125, v129, v125
	v_cvt_pk_bf16_f32 v124, v124, v125
	v_lshlrev_b32_e32 v125, 16, v225
	v_and_b32_e32 v128, 0xffff0000, v225
	v_add_f32_e32 v125, v130, v125
	v_add_f32_e32 v128, v131, v128
	v_cvt_pk_bf16_f32 v125, v125, v128
	v_lshlrev_b32_e32 v128, 16, v226
	v_add_f32_e32 v126, v126, v128
	v_and_b32_e32 v128, 0xffff0000, v226
	v_add_f32_e32 v127, v127, v128
	v_cvt_pk_bf16_f32 v126, v126, v127
	v_lshlrev_b32_e32 v127, 16, v227
	v_and_b32_e32 v128, 0xffff0000, v227
	v_add_f32_e32 v127, v140, v127
	v_add_f32_e32 v128, v141, v128
	v_cvt_pk_bf16_f32 v127, v127, v128
	global_store_dwordx4 v[134:135], v[124:127], off
	v_lshlrev_b32_e32 v128, 16, v124
	v_lshlrev_b32_e32 v129, 16, v125
	v_and_b32_e32 v124, 0xffff0000, v124
	v_and_b32_e32 v125, 0xffff0000, v125
	v_mul_f32_e32 v124, v124, v124
	v_mul_f32_e32 v125, v125, v125
	v_lshlrev_b32_e32 v130, 16, v126
	v_and_b32_e32 v126, 0xffff0000, v126
	v_fmac_f32_e32 v124, v128, v128
	v_fmac_f32_e32 v125, v129, v129
	v_add_f32_e32 v124, v124, v125
	v_mul_f32_e32 v125, v126, v126
	v_lshlrev_b32_e32 v131, 16, v127
	v_and_b32_e32 v127, 0xffff0000, v127
	v_fmac_f32_e32 v125, v130, v130
	v_add_f32_e32 v124, v124, v125
	v_mul_f32_e32 v125, v127, v127
	v_fmac_f32_e32 v125, v131, v131
	v_add_f32_e32 v130, v124, v125
	v_pk_mul_f32 v[128:129], v[58:59], v[118:119]
	v_pk_mul_f32 v[118:119], v[56:57], v[116:117]
	v_pk_mul_f32 v[122:123], v[50:51], v[122:123]
	s_waitcnt vmcnt(8)
	v_lshlrev_b32_e32 v116, 16, v228
	v_and_b32_e32 v117, 0xffff0000, v228
	v_add_f32_e32 v116, v120, v116
	v_add_f32_e32 v117, v121, v117
	v_cvt_pk_bf16_f32 v116, v116, v117
	v_lshlrev_b32_e32 v117, 16, v229
	v_and_b32_e32 v120, 0xffff0000, v229
	v_add_f32_e32 v117, v122, v117
	v_add_f32_e32 v120, v123, v120
	v_cvt_pk_bf16_f32 v117, v117, v120
	v_lshlrev_b32_e32 v120, 16, v230
	v_add_f32_e32 v118, v118, v120
	v_and_b32_e32 v120, 0xffff0000, v230
	v_add_f32_e32 v119, v119, v120
	v_cvt_pk_bf16_f32 v118, v118, v119
	v_lshlrev_b32_e32 v119, 16, v231
	v_and_b32_e32 v120, 0xffff0000, v231
	v_add_f32_e32 v119, v128, v119
	v_add_f32_e32 v120, v129, v120
	v_cvt_pk_bf16_f32 v119, v119, v120
	global_store_dwordx4 v[134:135], v[116:119], off offset:256
	s_mov_b64 s[20:21], 0x58000
	v_lshl_add_u64 v[220:221], v[204:205], 0, s[20:21]
	global_load_dwordx4 v[224:227], v[220:221], off
	global_load_dwordx4 v[228:231], v[220:221], off offset:256
	v_lshlrev_b32_e32 v120, 16, v116
	v_lshlrev_b32_e32 v121, 16, v117
	v_and_b32_e32 v116, 0xffff0000, v116
	v_and_b32_e32 v117, 0xffff0000, v117
	v_mul_f32_e32 v116, v116, v116
	v_mul_f32_e32 v117, v117, v117
	v_lshlrev_b32_e32 v122, 16, v118
	v_and_b32_e32 v118, 0xffff0000, v118
	v_fmac_f32_e32 v116, v120, v120
	v_fmac_f32_e32 v117, v121, v121
	v_add_f32_e32 v116, v116, v117
	v_mul_f32_e32 v117, v118, v118
	v_lshlrev_b32_e32 v123, 16, v119
	v_and_b32_e32 v119, 0xffff0000, v119
	v_fmac_f32_e32 v117, v122, v122
	v_add_f32_e32 v116, v116, v117
	v_mul_f32_e32 v117, v119, v119
	v_fmac_f32_e32 v117, v123, v123
	v_add_f32_e32 v116, v116, v117
	v_add_f32_e32 v116, v130, v116
	ds_bpermute_b32 v117, v152, v116
	s_waitcnt lgkmcnt(0)
	v_add_f32_e32 v116, v116, v117
	ds_bpermute_b32 v117, v153, v116
	s_and_saveexec_b64 s[4:5], s[42:43]
	s_cbranch_execz .LBB0_1193
	v_readlane_b32 s24, v253, 54
	s_waitcnt lgkmcnt(0)
	v_add_f32_e32 v118, v116, v117
	s_lshl_b32 s20, s87, 2
	v_lshlrev_b64 v[116:117], 6, v[132:133]
	v_readlane_b32 s25, v253, 55
	s_ashr_i32 s21, s20, 31
	s_lshl_b32 s30, s82, 2
	v_lshl_add_u64 v[116:117], s[24:25], 0, v[116:117]
	v_lshl_add_u64 v[116:117], s[20:21], 2, v[116:117]
	v_lshl_add_u64 v[116:117], v[116:117], 0, s[30:31]
	global_store_dword v[116:117], v118, off
; __device__ __forceinline__ unsigned cvt_pk_bf16(float lo, float hi) { unsigned r; asm volatile("v_cvt_pk_bf16_f32 %0, %1, %2" : "=v"(r) : "v"(lo), "v"(hi)); return r; }
;     __device__ __forceinline__ void operator()(const pg8::f32x4 (&acc)[2][2][4][2], const pg8::Unit& u, int wr, int wc, int fr, int fq) const {
;     ...
;             for (int m = 0; m < 4; ++m) { const size_t row = (size_t)(u.pm * 256 + rowoff + ai * 128 + wr * 64 + m * 16 + fr); bf16_t* rowp = X + row * 1024 + col0; float sq = 0.f;
; #pragma unroll
;                 for (int bj = 0; bj < 2; ++bj) { pg8::u32x4* ptr = (pg8::u32x4*)(rowp + bj * 128); const pg8::u32x4 xo = *ptr;
;                     const f32x4 v0 = gv[bj][0] * (acc[ai][bj][m][0] + bv[bj][0]), v1 = gv[bj][1] * (acc[ai][bj][m][1] + bv[bj][1]);
;                     pg8::u32x4 w;
;                     w.x = pg8::cvt_pk_bf16(bf2f(xo.x & 0xffffu) + v0[0], bf2f(xo.x >> 16) + v0[1]); w.y = pg8::cvt_pk_bf16(bf2f(xo.y & 0xffffu) + v0[2], bf2f(xo.y >> 16) + v0[3]);
;                     w.z = pg8::cvt_pk_bf16(bf2f(xo.z & 0xffffu) + v1[0], bf2f(xo.z >> 16) + v1[1]); w.w = pg8::cvt_pk_bf16(bf2f(xo.w & 0xffffu) + v1[2], bf2f(xo.w >> 16) + v1[3]);
;                     *ptr = w;
;                     { const float r0 = bf2f(w.x & 0xffffu), r1 = bf2f(w.x >> 16), r2 = bf2f(w.y & 0xffffu), r3 = bf2f(w.y >> 16), r4 = bf2f(w.z & 0xffffu), r5 = bf2f(w.z >> 16), r6 = bf2f(w.w & 0xffffu), r7 = bf2f(w.w >> 16);
;                       sq += (r0 * r0 + r1 * r1) + (r2 * r2 + r3 * r3) + (r4 * r4 + r5 * r5) + (r6 * r6 + r7 * r7); } }
;                 sq += __shfl_xor(sq, 16); sq += __shfl_xor(sq, 32);
;                 if (fq == 0) ssq[row * 16 + u.pn * 4 + wc] = sq; }
.LBB0_1193:
	s_or_b64 exec, exec, s[4:5]
	v_add_u32_e32 v116, s14, v184
	s_waitcnt lgkmcnt(0)
	v_ashrrev_i32_e32 v117, 31, v116
	v_readlane_b32 s4, v250, 6
	v_lshlrev_b64 v[118:119], 11, v[116:117]
	v_readlane_b32 s5, v250, 7
	v_pk_add_f32 v[112:113], v[112:113], v[52:53]
	v_pk_add_f32 v[110:111], v[110:111], v[46:47]
	v_lshl_add_u64 v[118:119], s[4:5], 0, v[118:119]
	v_lshl_add_u64 v[118:119], v[174:175], 1, v[118:119]
	v_pk_add_f32 v[108:109], v[108:109], v[44:45]
	v_pk_mul_f32 v[112:113], v[60:61], v[112:113]
	v_pk_mul_f32 v[124:125], v[66:67], v[110:111]
	v_pk_mul_f32 v[110:111], v[64:65], v[108:109]
	v_pk_add_f32 v[114:115], v[114:115], v[54:55]
	v_pk_add_f32 v[104:105], v[104:105], v[40:41]
	v_pk_mul_f32 v[114:115], v[62:63], v[114:115]
	v_pk_add_f32 v[102:103], v[102:103], v[38:39]
	v_pk_add_f32 v[100:101], v[100:101], v[36:37]
	v_pk_mul_f32 v[104:105], v[48:49], v[104:105]
	v_pk_add_f32 v[106:107], v[106:107], v[42:43]
	s_waitcnt vmcnt(9)
	v_lshlrev_b32_e32 v108, 16, v232
	v_and_b32_e32 v109, 0xffff0000, v232
	v_add_f32_e32 v108, v112, v108
	v_add_f32_e32 v109, v113, v109
	v_cvt_pk_bf16_f32 v108, v108, v109
	v_lshlrev_b32_e32 v109, 16, v233
	v_and_b32_e32 v112, 0xffff0000, v233
	v_add_f32_e32 v109, v114, v109
	v_add_f32_e32 v112, v115, v112
	v_cvt_pk_bf16_f32 v109, v109, v112
	v_lshlrev_b32_e32 v112, 16, v234
	v_add_f32_e32 v110, v110, v112
	v_and_b32_e32 v112, 0xffff0000, v234
	v_add_f32_e32 v111, v111, v112
	v_cvt_pk_bf16_f32 v110, v110, v111
	v_lshlrev_b32_e32 v111, 16, v235
	v_and_b32_e32 v112, 0xffff0000, v235
	v_add_f32_e32 v111, v124, v111
	v_add_f32_e32 v112, v125, v112
	v_cvt_pk_bf16_f32 v111, v111, v112
	global_store_dwordx4 v[118:119], v[108:111], off
	v_lshlrev_b32_e32 v112, 16, v108
	v_lshlrev_b32_e32 v113, 16, v109
	v_and_b32_e32 v108, 0xffff0000, v108
	v_and_b32_e32 v109, 0xffff0000, v109
	v_mul_f32_e32 v108, v108, v108
	v_mul_f32_e32 v109, v109, v109
	v_lshlrev_b32_e32 v114, 16, v110
	v_and_b32_e32 v110, 0xffff0000, v110
	v_fmac_f32_e32 v108, v112, v112
	v_fmac_f32_e32 v109, v113, v113
	v_add_f32_e32 v108, v108, v109
	v_mul_f32_e32 v109, v110, v110
	v_lshlrev_b32_e32 v115, 16, v111
	v_and_b32_e32 v111, 0xffff0000, v111
	v_fmac_f32_e32 v109, v114, v114
	v_add_f32_e32 v108, v108, v109
	v_mul_f32_e32 v109, v111, v111
	v_fmac_f32_e32 v109, v115, v115
	v_add_f32_e32 v114, v108, v109
	v_pk_mul_f32 v[112:113], v[58:59], v[102:103]
	v_pk_mul_f32 v[102:103], v[56:57], v[100:101]
	v_pk_mul_f32 v[106:107], v[50:51], v[106:107]
	s_waitcnt vmcnt(8)
	v_lshlrev_b32_e32 v100, 16, v236
	v_and_b32_e32 v101, 0xffff0000, v236
	v_add_f32_e32 v100, v104, v100
	v_add_f32_e32 v101, v105, v101
	v_cvt_pk_bf16_f32 v100, v100, v101
	v_lshlrev_b32_e32 v101, 16, v237
	v_and_b32_e32 v104, 0xffff0000, v237
	v_add_f32_e32 v101, v106, v101
	v_add_f32_e32 v104, v107, v104
	v_cvt_pk_bf16_f32 v101, v101, v104
	v_lshlrev_b32_e32 v104, 16, v238
	v_add_f32_e32 v102, v102, v104
	v_and_b32_e32 v104, 0xffff0000, v238
	v_add_f32_e32 v103, v103, v104
	v_cvt_pk_bf16_f32 v102, v102, v103
	v_lshlrev_b32_e32 v103, 16, v239
	v_and_b32_e32 v104, 0xffff0000, v239
	v_add_f32_e32 v103, v112, v103
	v_add_f32_e32 v104, v113, v104
	v_cvt_pk_bf16_f32 v103, v103, v104
	global_store_dwordx4 v[118:119], v[100:103], off offset:256
	v_lshlrev_b32_e32 v104, 16, v100
	v_lshlrev_b32_e32 v105, 16, v101
	v_and_b32_e32 v100, 0xffff0000, v100
	v_and_b32_e32 v101, 0xffff0000, v101
	v_mul_f32_e32 v100, v100, v100
	v_mul_f32_e32 v101, v101, v101
	v_lshlrev_b32_e32 v106, 16, v102
	v_and_b32_e32 v102, 0xffff0000, v102
	v_fmac_f32_e32 v100, v104, v104
	v_fmac_f32_e32 v101, v105, v105
	v_add_f32_e32 v100, v100, v101
	v_mul_f32_e32 v101, v102, v102
	v_lshlrev_b32_e32 v107, 16, v103
	v_and_b32_e32 v103, 0xffff0000, v103
	v_fmac_f32_e32 v101, v106, v106
	v_add_f32_e32 v100, v100, v101
	v_mul_f32_e32 v101, v103, v103
	v_fmac_f32_e32 v101, v107, v107
	v_add_f32_e32 v100, v100, v101
	v_add_f32_e32 v100, v114, v100
	ds_bpermute_b32 v101, v152, v100
	s_waitcnt lgkmcnt(0)
	v_add_f32_e32 v100, v100, v101
	ds_bpermute_b32 v101, v153, v100
	s_and_saveexec_b64 s[4:5], s[42:43]
	s_cbranch_execz .LBB0_1195
	v_readlane_b32 s24, v253, 54
	s_waitcnt lgkmcnt(0)
	v_add_f32_e32 v102, v100, v101
	s_lshl_b32 s20, s87, 2
	v_lshlrev_b64 v[100:101], 6, v[116:117]
	v_readlane_b32 s25, v253, 55
	s_ashr_i32 s21, s20, 31
	s_lshl_b32 s30, s82, 2
	v_lshl_add_u64 v[100:101], s[24:25], 0, v[100:101]
	v_lshl_add_u64 v[100:101], s[20:21], 2, v[100:101]
	v_lshl_add_u64 v[100:101], v[100:101], 0, s[30:31]
	global_store_dword v[100:101], v102, off
; __device__ __forceinline__ unsigned cvt_pk_bf16(float lo, float hi) { unsigned r; asm volatile("v_cvt_pk_bf16_f32 %0, %1, %2" : "=v"(r) : "v"(lo), "v"(hi)); return r; }
;     __device__ __forceinline__ void operator()(const pg8::f32x4 (&acc)[2][2][4][2], const pg8::Unit& u, int wr, int wc, int fr, int fq) const {
;     ...
;             for (int m = 0; m < 4; ++m) { const size_t row = (size_t)(u.pm * 256 + rowoff + ai * 128 + wr * 64 + m * 16 + fr); bf16_t* rowp = X + row * 1024 + col0; float sq = 0.f;
; #pragma unroll
;                 for (int bj = 0; bj < 2; ++bj) { pg8::u32x4* ptr = (pg8::u32x4*)(rowp + bj * 128); const pg8::u32x4 xo = *ptr;
;                     const f32x4 v0 = gv[bj][0] * (acc[ai][bj][m][0] + bv[bj][0]), v1 = gv[bj][1] * (acc[ai][bj][m][1] + bv[bj][1]);
;                     pg8::u32x4 w;
;                     w.x = pg8::cvt_pk_bf16(bf2f(xo.x & 0xffffu) + v0[0], bf2f(xo.x >> 16) + v0[1]); w.y = pg8::cvt_pk_bf16(bf2f(xo.y & 0xffffu) + v0[2], bf2f(xo.y >> 16) + v0[3]);
;                     w.z = pg8::cvt_pk_bf16(bf2f(xo.z & 0xffffu) + v1[0], bf2f(xo.z >> 16) + v1[1]); w.w = pg8::cvt_pk_bf16(bf2f(xo.w & 0xffffu) + v1[2], bf2f(xo.w >> 16) + v1[3]);
;                     *ptr = w;
;                     { const float r0 = bf2f(w.x & 0xffffu), r1 = bf2f(w.x >> 16), r2 = bf2f(w.y & 0xffffu), r3 = bf2f(w.y >> 16), r4 = bf2f(w.z & 0xffffu), r5 = bf2f(w.z >> 16), r6 = bf2f(w.w & 0xffffu), r7 = bf2f(w.w >> 16);
;                       sq += (r0 * r0 + r1 * r1) + (r2 * r2 + r3 * r3) + (r4 * r4 + r5 * r5) + (r6 * r6 + r7 * r7); } }
;                 sq += __shfl_xor(sq, 16); sq += __shfl_xor(sq, 32);
;                 if (fq == 0) ssq[row * 16 + u.pn * 4 + wc] = sq; }
.LBB0_1195:
	s_or_b64 exec, exec, s[4:5]
	v_add_u32_e32 v100, 0x80, v176
	s_waitcnt lgkmcnt(0)
	v_ashrrev_i32_e32 v101, 31, v100
	v_readlane_b32 s4, v250, 6
	v_lshlrev_b64 v[102:103], 11, v[100:101]
	v_readlane_b32 s5, v250, 7
	v_pk_add_f32 v[96:97], v[96:97], v[52:53]
	v_pk_add_f32 v[94:95], v[94:95], v[46:47]
	v_lshl_add_u64 v[102:103], s[4:5], 0, v[102:103]
	v_lshl_add_u64 v[102:103], v[174:175], 1, v[102:103]
	v_pk_add_f32 v[92:93], v[92:93], v[44:45]
	v_pk_mul_f32 v[96:97], v[60:61], v[96:97]
	v_pk_mul_f32 v[108:109], v[66:67], v[94:95]
	v_pk_mul_f32 v[94:95], v[64:65], v[92:93]
	v_pk_add_f32 v[98:99], v[98:99], v[54:55]
	v_pk_add_f32 v[88:89], v[88:89], v[40:41]
	v_pk_mul_f32 v[98:99], v[62:63], v[98:99]
	v_pk_add_f32 v[86:87], v[86:87], v[38:39]
	v_pk_add_f32 v[84:85], v[84:85], v[36:37]
	v_pk_mul_f32 v[88:89], v[48:49], v[88:89]
	v_pk_add_f32 v[90:91], v[90:91], v[42:43]
	s_waitcnt vmcnt(7)
	v_lshlrev_b32_e32 v92, 16, v216
	v_and_b32_e32 v93, 0xffff0000, v216
	v_add_f32_e32 v92, v96, v92
	v_add_f32_e32 v93, v97, v93
	v_cvt_pk_bf16_f32 v92, v92, v93
	v_lshlrev_b32_e32 v93, 16, v217
	v_and_b32_e32 v96, 0xffff0000, v217
	v_add_f32_e32 v93, v98, v93
	v_add_f32_e32 v96, v99, v96
	v_cvt_pk_bf16_f32 v93, v93, v96
	v_lshlrev_b32_e32 v96, 16, v218
	v_add_f32_e32 v94, v94, v96
	v_and_b32_e32 v96, 0xffff0000, v218
	v_add_f32_e32 v95, v95, v96
	v_cvt_pk_bf16_f32 v94, v94, v95
	v_lshlrev_b32_e32 v95, 16, v219
	v_and_b32_e32 v96, 0xffff0000, v219
	v_add_f32_e32 v95, v108, v95
	v_add_f32_e32 v96, v109, v96
	v_cvt_pk_bf16_f32 v95, v95, v96
	global_store_dwordx4 v[102:103], v[92:95], off
	v_lshlrev_b32_e32 v96, 16, v92
	v_lshlrev_b32_e32 v97, 16, v93
	v_and_b32_e32 v92, 0xffff0000, v92
	v_and_b32_e32 v93, 0xffff0000, v93
	v_mul_f32_e32 v92, v92, v92
	v_mul_f32_e32 v93, v93, v93
	v_lshlrev_b32_e32 v98, 16, v94
	v_and_b32_e32 v94, 0xffff0000, v94
	v_fmac_f32_e32 v92, v96, v96
	v_fmac_f32_e32 v93, v97, v97
	v_add_f32_e32 v92, v92, v93
	v_mul_f32_e32 v93, v94, v94
	v_lshlrev_b32_e32 v99, 16, v95
	v_and_b32_e32 v95, 0xffff0000, v95
	v_fmac_f32_e32 v93, v98, v98
	v_add_f32_e32 v92, v92, v93
	v_mul_f32_e32 v93, v95, v95
	v_fmac_f32_e32 v93, v99, v99
	v_add_f32_e32 v98, v92, v93
	v_pk_mul_f32 v[96:97], v[58:59], v[86:87]
	v_pk_mul_f32 v[86:87], v[56:57], v[84:85]
	v_pk_mul_f32 v[90:91], v[50:51], v[90:91]
	s_waitcnt vmcnt(6)
	v_lshlrev_b32_e32 v84, 16, v244
	v_and_b32_e32 v85, 0xffff0000, v244
	v_add_f32_e32 v84, v88, v84
	v_add_f32_e32 v85, v89, v85
	v_cvt_pk_bf16_f32 v84, v84, v85
	v_lshlrev_b32_e32 v85, 16, v245
	v_and_b32_e32 v88, 0xffff0000, v245
	v_add_f32_e32 v85, v90, v85
	v_add_f32_e32 v88, v91, v88
	v_cvt_pk_bf16_f32 v85, v85, v88
	v_lshlrev_b32_e32 v88, 16, v246
	v_add_f32_e32 v86, v86, v88
	v_and_b32_e32 v88, 0xffff0000, v246
	v_add_f32_e32 v87, v87, v88
	v_cvt_pk_bf16_f32 v86, v86, v87
	v_lshlrev_b32_e32 v87, 16, v247
	v_and_b32_e32 v88, 0xffff0000, v247
	v_add_f32_e32 v87, v96, v87
	v_add_f32_e32 v88, v97, v88
	v_cvt_pk_bf16_f32 v87, v87, v88
	global_store_dwordx4 v[102:103], v[84:87], off offset:256
	v_lshlrev_b32_e32 v88, 16, v84
	v_lshlrev_b32_e32 v89, 16, v85
	v_and_b32_e32 v84, 0xffff0000, v84
	v_and_b32_e32 v85, 0xffff0000, v85
	v_mul_f32_e32 v84, v84, v84
	v_mul_f32_e32 v85, v85, v85
	v_lshlrev_b32_e32 v90, 16, v86
	v_and_b32_e32 v86, 0xffff0000, v86
	v_fmac_f32_e32 v84, v88, v88
	v_fmac_f32_e32 v85, v89, v89
	v_add_f32_e32 v84, v84, v85
	v_mul_f32_e32 v85, v86, v86
	v_lshlrev_b32_e32 v91, 16, v87
	v_and_b32_e32 v87, 0xffff0000, v87
	v_fmac_f32_e32 v85, v90, v90
	v_add_f32_e32 v84, v84, v85
	v_mul_f32_e32 v85, v87, v87
	v_fmac_f32_e32 v85, v91, v91
	v_add_f32_e32 v84, v84, v85
	v_add_f32_e32 v84, v98, v84
	ds_bpermute_b32 v85, v152, v84
	s_waitcnt lgkmcnt(0)
	v_add_f32_e32 v84, v84, v85
	ds_bpermute_b32 v85, v153, v84
	s_and_saveexec_b64 s[4:5], s[42:43]
	s_cbranch_execz .LBB0_1197
	v_readlane_b32 s24, v253, 54
	s_waitcnt lgkmcnt(0)
	v_add_f32_e32 v86, v84, v85
	s_lshl_b32 s20, s87, 2
	v_lshlrev_b64 v[84:85], 6, v[100:101]
	v_readlane_b32 s25, v253, 55
	s_ashr_i32 s21, s20, 31
	s_lshl_b32 s30, s82, 2
	v_lshl_add_u64 v[84:85], s[24:25], 0, v[84:85]
	v_lshl_add_u64 v[84:85], s[20:21], 2, v[84:85]
	v_lshl_add_u64 v[84:85], v[84:85], 0, s[30:31]
	global_store_dword v[84:85], v86, off
; __device__ __forceinline__ unsigned cvt_pk_bf16(float lo, float hi) { unsigned r; asm volatile("v_cvt_pk_bf16_f32 %0, %1, %2" : "=v"(r) : "v"(lo), "v"(hi)); return r; }
;     __device__ __forceinline__ void operator()(const pg8::f32x4 (&acc)[2][2][4][2], const pg8::Unit& u, int wr, int wc, int fr, int fq) const {
;     ...
;             for (int m = 0; m < 4; ++m) { const size_t row = (size_t)(u.pm * 256 + rowoff + ai * 128 + wr * 64 + m * 16 + fr); bf16_t* rowp = X + row * 1024 + col0; float sq = 0.f;
; #pragma unroll
;                 for (int bj = 0; bj < 2; ++bj) { pg8::u32x4* ptr = (pg8::u32x4*)(rowp + bj * 128); const pg8::u32x4 xo = *ptr;
;                     const f32x4 v0 = gv[bj][0] * (acc[ai][bj][m][0] + bv[bj][0]), v1 = gv[bj][1] * (acc[ai][bj][m][1] + bv[bj][1]);
;                     pg8::u32x4 w;
;                     w.x = pg8::cvt_pk_bf16(bf2f(xo.x & 0xffffu) + v0[0], bf2f(xo.x >> 16) + v0[1]); w.y = pg8::cvt_pk_bf16(bf2f(xo.y & 0xffffu) + v0[2], bf2f(xo.y >> 16) + v0[3]);
;                     w.z = pg8::cvt_pk_bf16(bf2f(xo.z & 0xffffu) + v1[0], bf2f(xo.z >> 16) + v1[1]); w.w = pg8::cvt_pk_bf16(bf2f(xo.w & 0xffffu) + v1[2], bf2f(xo.w >> 16) + v1[3]);
;                     *ptr = w;
;                     { const float r0 = bf2f(w.x & 0xffffu), r1 = bf2f(w.x >> 16), r2 = bf2f(w.y & 0xffffu), r3 = bf2f(w.y >> 16), r4 = bf2f(w.z & 0xffffu), r5 = bf2f(w.z >> 16), r6 = bf2f(w.w & 0xffffu), r7 = bf2f(w.w >> 16);
;                       sq += (r0 * r0 + r1 * r1) + (r2 * r2 + r3 * r3) + (r4 * r4 + r5 * r5) + (r6 * r6 + r7 * r7); } }
;                 sq += __shfl_xor(sq, 16); sq += __shfl_xor(sq, 32);
;                 if (fq == 0) ssq[row * 16 + u.pn * 4 + wc] = sq; }
.LBB0_1197:
	s_or_b64 exec, exec, s[4:5]
	v_add_u32_e32 v84, 0x90, v176
	s_waitcnt lgkmcnt(0)
	v_ashrrev_i32_e32 v85, 31, v84
	v_readlane_b32 s4, v250, 6
	v_lshlrev_b64 v[86:87], 11, v[84:85]
	v_readlane_b32 s5, v250, 7
	v_pk_add_f32 v[80:81], v[80:81], v[52:53]
	v_pk_add_f32 v[78:79], v[78:79], v[46:47]
	v_lshl_add_u64 v[86:87], s[4:5], 0, v[86:87]
	v_lshl_add_u64 v[86:87], v[174:175], 1, v[86:87]
	v_pk_add_f32 v[76:77], v[76:77], v[44:45]
	v_pk_mul_f32 v[80:81], v[60:61], v[80:81]
	v_pk_mul_f32 v[92:93], v[66:67], v[78:79]
	v_pk_mul_f32 v[78:79], v[64:65], v[76:77]
	v_pk_add_f32 v[82:83], v[82:83], v[54:55]
	v_pk_add_f32 v[72:73], v[72:73], v[40:41]
	v_pk_mul_f32 v[82:83], v[62:63], v[82:83]
	v_pk_add_f32 v[70:71], v[70:71], v[38:39]
	v_pk_add_f32 v[68:69], v[68:69], v[36:37]
	v_pk_mul_f32 v[72:73], v[48:49], v[72:73]
	v_pk_add_f32 v[74:75], v[74:75], v[42:43]
	s_waitcnt vmcnt(5)
	v_lshlrev_b32_e32 v76, 16, v192
	v_and_b32_e32 v77, 0xffff0000, v192
	v_add_f32_e32 v76, v80, v76
	v_add_f32_e32 v77, v81, v77
	v_cvt_pk_bf16_f32 v76, v76, v77
	v_lshlrev_b32_e32 v77, 16, v193
	v_and_b32_e32 v80, 0xffff0000, v193
	v_add_f32_e32 v77, v82, v77
	v_add_f32_e32 v80, v83, v80
	v_cvt_pk_bf16_f32 v77, v77, v80
	v_lshlrev_b32_e32 v80, 16, v194
	v_add_f32_e32 v78, v78, v80
	v_and_b32_e32 v80, 0xffff0000, v194
	v_add_f32_e32 v79, v79, v80
	v_cvt_pk_bf16_f32 v78, v78, v79
	v_lshlrev_b32_e32 v79, 16, v195
	v_and_b32_e32 v80, 0xffff0000, v195
	v_add_f32_e32 v79, v92, v79
	v_add_f32_e32 v80, v93, v80
	v_cvt_pk_bf16_f32 v79, v79, v80
	global_store_dwordx4 v[86:87], v[76:79], off
	v_lshlrev_b32_e32 v80, 16, v76
	v_lshlrev_b32_e32 v81, 16, v77
	v_and_b32_e32 v76, 0xffff0000, v76
	v_and_b32_e32 v77, 0xffff0000, v77
	v_mul_f32_e32 v76, v76, v76
	v_mul_f32_e32 v77, v77, v77
	v_lshlrev_b32_e32 v82, 16, v78
	v_and_b32_e32 v78, 0xffff0000, v78
	v_fmac_f32_e32 v76, v80, v80
	v_fmac_f32_e32 v77, v81, v81
	v_add_f32_e32 v76, v76, v77
	v_mul_f32_e32 v77, v78, v78
	v_lshlrev_b32_e32 v83, 16, v79
	v_and_b32_e32 v79, 0xffff0000, v79
	v_fmac_f32_e32 v77, v82, v82
	v_add_f32_e32 v76, v76, v77
	v_mul_f32_e32 v77, v79, v79
	v_fmac_f32_e32 v77, v83, v83
	v_add_f32_e32 v82, v76, v77
	v_pk_mul_f32 v[80:81], v[58:59], v[70:71]
	v_pk_mul_f32 v[70:71], v[56:57], v[68:69]
	v_pk_mul_f32 v[74:75], v[50:51], v[74:75]
	s_waitcnt vmcnt(4)
	v_lshlrev_b32_e32 v68, 16, v196
	v_and_b32_e32 v69, 0xffff0000, v196
	v_add_f32_e32 v68, v72, v68
	v_add_f32_e32 v69, v73, v69
	v_cvt_pk_bf16_f32 v68, v68, v69
	v_lshlrev_b32_e32 v69, 16, v197
	v_and_b32_e32 v72, 0xffff0000, v197
	v_add_f32_e32 v69, v74, v69
	v_add_f32_e32 v72, v75, v72
	v_cvt_pk_bf16_f32 v69, v69, v72
	v_lshlrev_b32_e32 v72, 16, v198
	v_add_f32_e32 v70, v70, v72
	v_and_b32_e32 v72, 0xffff0000, v198
	v_add_f32_e32 v71, v71, v72
	v_cvt_pk_bf16_f32 v70, v70, v71
	v_lshlrev_b32_e32 v71, 16, v199
	v_and_b32_e32 v72, 0xffff0000, v199
	v_add_f32_e32 v71, v80, v71
	v_add_f32_e32 v72, v81, v72
	v_cvt_pk_bf16_f32 v71, v71, v72
	global_store_dwordx4 v[86:87], v[68:71], off offset:256
	v_lshlrev_b32_e32 v72, 16, v68
	v_lshlrev_b32_e32 v73, 16, v69
	v_and_b32_e32 v68, 0xffff0000, v68
	v_and_b32_e32 v69, 0xffff0000, v69
	v_mul_f32_e32 v68, v68, v68
	v_mul_f32_e32 v69, v69, v69
	v_lshlrev_b32_e32 v74, 16, v70
	v_and_b32_e32 v70, 0xffff0000, v70
	v_fmac_f32_e32 v68, v72, v72
	v_fmac_f32_e32 v69, v73, v73
	v_add_f32_e32 v68, v68, v69
	v_mul_f32_e32 v69, v70, v70
	v_lshlrev_b32_e32 v75, 16, v71
	v_and_b32_e32 v71, 0xffff0000, v71
	v_fmac_f32_e32 v69, v74, v74
	v_add_f32_e32 v68, v68, v69
	v_mul_f32_e32 v69, v71, v71
	v_fmac_f32_e32 v69, v75, v75
	v_add_f32_e32 v68, v68, v69
	v_add_f32_e32 v68, v82, v68
	ds_bpermute_b32 v69, v152, v68
	s_waitcnt lgkmcnt(0)
	v_add_f32_e32 v68, v68, v69
	ds_bpermute_b32 v69, v153, v68
	s_and_saveexec_b64 s[4:5], s[42:43]
	s_cbranch_execz .LBB0_1199
	v_readlane_b32 s24, v253, 54
	s_waitcnt lgkmcnt(0)
	v_add_f32_e32 v70, v68, v69
	s_lshl_b32 s20, s87, 2
	v_lshlrev_b64 v[68:69], 6, v[84:85]
	v_readlane_b32 s25, v253, 55
	s_ashr_i32 s21, s20, 31
	s_lshl_b32 s30, s82, 2
	v_lshl_add_u64 v[68:69], s[24:25], 0, v[68:69]
	v_lshl_add_u64 v[68:69], s[20:21], 2, v[68:69]
	v_lshl_add_u64 v[68:69], v[68:69], 0, s[30:31]
	global_store_dword v[68:69], v70, off
; __device__ __forceinline__ unsigned cvt_pk_bf16(float lo, float hi) { unsigned r; asm volatile("v_cvt_pk_bf16_f32 %0, %1, %2" : "=v"(r) : "v"(lo), "v"(hi)); return r; }
;     __device__ __forceinline__ void operator()(const pg8::f32x4 (&acc)[2][2][4][2], const pg8::Unit& u, int wr, int wc, int fr, int fq) const {
;     ...
;             for (int m = 0; m < 4; ++m) { const size_t row = (size_t)(u.pm * 256 + rowoff + ai * 128 + wr * 64 + m * 16 + fr); bf16_t* rowp = X + row * 1024 + col0; float sq = 0.f;
; #pragma unroll
;                 for (int bj = 0; bj < 2; ++bj) { pg8::u32x4* ptr = (pg8::u32x4*)(rowp + bj * 128); const pg8::u32x4 xo = *ptr;
;                     const f32x4 v0 = gv[bj][0] * (acc[ai][bj][m][0] + bv[bj][0]), v1 = gv[bj][1] * (acc[ai][bj][m][1] + bv[bj][1]);
;                     pg8::u32x4 w;
;                     w.x = pg8::cvt_pk_bf16(bf2f(xo.x & 0xffffu) + v0[0], bf2f(xo.x >> 16) + v0[1]); w.y = pg8::cvt_pk_bf16(bf2f(xo.y & 0xffffu) + v0[2], bf2f(xo.y >> 16) + v0[3]);
;                     w.z = pg8::cvt_pk_bf16(bf2f(xo.z & 0xffffu) + v1[0], bf2f(xo.z >> 16) + v1[1]); w.w = pg8::cvt_pk_bf16(bf2f(xo.w & 0xffffu) + v1[2], bf2f(xo.w >> 16) + v1[3]);
;                     *ptr = w;
;                     { const float r0 = bf2f(w.x & 0xffffu), r1 = bf2f(w.x >> 16), r2 = bf2f(w.y & 0xffffu), r3 = bf2f(w.y >> 16), r4 = bf2f(w.z & 0xffffu), r5 = bf2f(w.z >> 16), r6 = bf2f(w.w & 0xffffu), r7 = bf2f(w.w >> 16);
;                       sq += (r0 * r0 + r1 * r1) + (r2 * r2 + r3 * r3) + (r4 * r4 + r5 * r5) + (r6 * r6 + r7 * r7); } }
;                 sq += __shfl_xor(sq, 16); sq += __shfl_xor(sq, 32);
;                 if (fq == 0) ssq[row * 16 + u.pn * 4 + wc] = sq; }
.LBB0_1199:
	s_or_b64 exec, exec, s[4:5]
	v_add_u32_e32 v68, 0xa0, v176
	s_waitcnt lgkmcnt(0)
	v_ashrrev_i32_e32 v69, 31, v68
	v_readlane_b32 s4, v250, 6
	v_lshlrev_b64 v[70:71], 11, v[68:69]
	v_readlane_b32 s5, v250, 7
	v_pk_add_f32 v[32:33], v[32:33], v[52:53]
	v_pk_add_f32 v[30:31], v[30:31], v[46:47]
	v_lshl_add_u64 v[70:71], s[4:5], 0, v[70:71]
	v_lshl_add_u64 v[70:71], v[174:175], 1, v[70:71]
	v_pk_add_f32 v[28:29], v[28:29], v[44:45]
	v_pk_mul_f32 v[32:33], v[60:61], v[32:33]
	v_pk_mul_f32 v[76:77], v[66:67], v[30:31]
	v_pk_mul_f32 v[30:31], v[64:65], v[28:29]
	v_pk_add_f32 v[34:35], v[34:35], v[54:55]
	v_pk_add_f32 v[24:25], v[24:25], v[40:41]
	v_pk_mul_f32 v[34:35], v[62:63], v[34:35]
	v_pk_add_f32 v[22:23], v[22:23], v[38:39]
	v_pk_add_f32 v[20:21], v[20:21], v[36:37]
	v_pk_mul_f32 v[24:25], v[48:49], v[24:25]
	v_pk_add_f32 v[26:27], v[26:27], v[42:43]
	s_waitcnt vmcnt(3)
	v_lshlrev_b32_e32 v28, 16, v200
	v_and_b32_e32 v29, 0xffff0000, v200
	v_add_f32_e32 v28, v32, v28
	v_add_f32_e32 v29, v33, v29
	v_cvt_pk_bf16_f32 v28, v28, v29
	v_lshlrev_b32_e32 v29, 16, v201
	v_and_b32_e32 v32, 0xffff0000, v201
	v_add_f32_e32 v29, v34, v29
	v_add_f32_e32 v32, v35, v32
	v_cvt_pk_bf16_f32 v29, v29, v32
	v_lshlrev_b32_e32 v32, 16, v202
	v_add_f32_e32 v30, v30, v32
	v_and_b32_e32 v32, 0xffff0000, v202
	v_add_f32_e32 v31, v31, v32
	v_cvt_pk_bf16_f32 v30, v30, v31
	v_lshlrev_b32_e32 v31, 16, v203
	v_and_b32_e32 v32, 0xffff0000, v203
	v_add_f32_e32 v31, v76, v31
	v_add_f32_e32 v32, v77, v32
	v_cvt_pk_bf16_f32 v31, v31, v32
	global_store_dwordx4 v[70:71], v[28:31], off
	v_lshlrev_b32_e32 v32, 16, v28
	v_lshlrev_b32_e32 v33, 16, v29
	v_and_b32_e32 v28, 0xffff0000, v28
	v_and_b32_e32 v29, 0xffff0000, v29
	v_mul_f32_e32 v28, v28, v28
	v_mul_f32_e32 v29, v29, v29
	v_lshlrev_b32_e32 v34, 16, v30
	v_and_b32_e32 v30, 0xffff0000, v30
	v_fmac_f32_e32 v28, v32, v32
	v_fmac_f32_e32 v29, v33, v33
	v_add_f32_e32 v28, v28, v29
	v_mul_f32_e32 v29, v30, v30
	v_lshlrev_b32_e32 v35, 16, v31
	v_and_b32_e32 v31, 0xffff0000, v31
	v_fmac_f32_e32 v29, v34, v34
	v_add_f32_e32 v28, v28, v29
	v_mul_f32_e32 v29, v31, v31
	v_fmac_f32_e32 v29, v35, v35
	v_add_f32_e32 v34, v28, v29
	v_pk_mul_f32 v[32:33], v[58:59], v[22:23]
	v_pk_mul_f32 v[22:23], v[56:57], v[20:21]
	v_pk_mul_f32 v[26:27], v[50:51], v[26:27]
	s_waitcnt vmcnt(2)
	v_lshlrev_b32_e32 v20, 16, v208
	v_and_b32_e32 v21, 0xffff0000, v208
	v_add_f32_e32 v20, v24, v20
	v_add_f32_e32 v21, v25, v21
	v_cvt_pk_bf16_f32 v20, v20, v21
	v_lshlrev_b32_e32 v21, 16, v209
	v_and_b32_e32 v24, 0xffff0000, v209
	v_add_f32_e32 v21, v26, v21
	v_add_f32_e32 v24, v27, v24
	v_cvt_pk_bf16_f32 v21, v21, v24
	v_lshlrev_b32_e32 v24, 16, v210
	v_add_f32_e32 v22, v22, v24
	v_and_b32_e32 v24, 0xffff0000, v210
	v_add_f32_e32 v23, v23, v24
	v_cvt_pk_bf16_f32 v22, v22, v23
	v_lshlrev_b32_e32 v23, 16, v211
	v_and_b32_e32 v24, 0xffff0000, v211
	v_add_f32_e32 v23, v32, v23
	v_add_f32_e32 v24, v33, v24
	v_cvt_pk_bf16_f32 v23, v23, v24
	global_store_dwordx4 v[70:71], v[20:23], off offset:256
	v_lshlrev_b32_e32 v24, 16, v20
	v_lshlrev_b32_e32 v25, 16, v21
	v_and_b32_e32 v20, 0xffff0000, v20
	v_and_b32_e32 v21, 0xffff0000, v21
	v_mul_f32_e32 v20, v20, v20
	v_mul_f32_e32 v21, v21, v21
	v_lshlrev_b32_e32 v26, 16, v22
	v_and_b32_e32 v22, 0xffff0000, v22
	v_fmac_f32_e32 v20, v24, v24
	v_fmac_f32_e32 v21, v25, v25
	v_add_f32_e32 v20, v20, v21
	v_mul_f32_e32 v21, v22, v22
	v_lshlrev_b32_e32 v27, 16, v23
	v_and_b32_e32 v23, 0xffff0000, v23
	v_fmac_f32_e32 v21, v26, v26
	v_add_f32_e32 v20, v20, v21
	v_mul_f32_e32 v21, v23, v23
	v_fmac_f32_e32 v21, v27, v27
	v_add_f32_e32 v20, v20, v21
	v_add_f32_e32 v20, v34, v20
	ds_bpermute_b32 v21, v152, v20
	s_waitcnt lgkmcnt(0)
	v_add_f32_e32 v20, v20, v21
	ds_bpermute_b32 v21, v153, v20
	s_and_saveexec_b64 s[4:5], s[42:43]
	s_cbranch_execz .LBB0_1201
	v_readlane_b32 s24, v253, 54
	s_waitcnt lgkmcnt(0)
	v_add_f32_e32 v22, v20, v21
	s_lshl_b32 s20, s87, 2
	v_lshlrev_b64 v[20:21], 6, v[68:69]
	v_readlane_b32 s25, v253, 55
	s_ashr_i32 s21, s20, 31
	s_lshl_b32 s30, s82, 2
	v_lshl_add_u64 v[20:21], s[24:25], 0, v[20:21]
	v_lshl_add_u64 v[20:21], s[20:21], 2, v[20:21]
	v_lshl_add_u64 v[20:21], v[20:21], 0, s[30:31]
	global_store_dword v[20:21], v22, off
; __device__ __forceinline__ unsigned cvt_pk_bf16(float lo, float hi) { unsigned r; asm volatile("v_cvt_pk_bf16_f32 %0, %1, %2" : "=v"(r) : "v"(lo), "v"(hi)); return r; }
;     __device__ __forceinline__ void operator()(const pg8::f32x4 (&acc)[2][2][4][2], const pg8::Unit& u, int wr, int wc, int fr, int fq) const {
;     ...
;             for (int m = 0; m < 4; ++m) { const size_t row = (size_t)(u.pm * 256 + rowoff + ai * 128 + wr * 64 + m * 16 + fr); bf16_t* rowp = X + row * 1024 + col0; float sq = 0.f;
; #pragma unroll
;                 for (int bj = 0; bj < 2; ++bj) { pg8::u32x4* ptr = (pg8::u32x4*)(rowp + bj * 128); const pg8::u32x4 xo = *ptr;
;                     const f32x4 v0 = gv[bj][0] * (acc[ai][bj][m][0] + bv[bj][0]), v1 = gv[bj][1] * (acc[ai][bj][m][1] + bv[bj][1]);
;                     pg8::u32x4 w;
;                     w.x = pg8::cvt_pk_bf16(bf2f(xo.x & 0xffffu) + v0[0], bf2f(xo.x >> 16) + v0[1]); w.y = pg8::cvt_pk_bf16(bf2f(xo.y & 0xffffu) + v0[2], bf2f(xo.y >> 16) + v0[3]);
;                     w.z = pg8::cvt_pk_bf16(bf2f(xo.z & 0xffffu) + v1[0], bf2f(xo.z >> 16) + v1[1]); w.w = pg8::cvt_pk_bf16(bf2f(xo.w & 0xffffu) + v1[2], bf2f(xo.w >> 16) + v1[3]);
;                     *ptr = w;
;                     { const float r0 = bf2f(w.x & 0xffffu), r1 = bf2f(w.x >> 16), r2 = bf2f(w.y & 0xffffu), r3 = bf2f(w.y >> 16), r4 = bf2f(w.z & 0xffffu), r5 = bf2f(w.z >> 16), r6 = bf2f(w.w & 0xffffu), r7 = bf2f(w.w >> 16);
;                       sq += (r0 * r0 + r1 * r1) + (r2 * r2 + r3 * r3) + (r4 * r4 + r5 * r5) + (r6 * r6 + r7 * r7); } }
;                 sq += __shfl_xor(sq, 16); sq += __shfl_xor(sq, 32);
;                 if (fq == 0) ssq[row * 16 + u.pn * 4 + wc] = sq; }
.LBB0_1201:
	s_or_b64 exec, exec, s[4:5]
	v_add_u32_e32 v20, 0xb0, v176
	s_waitcnt lgkmcnt(0)
	v_ashrrev_i32_e32 v21, 31, v20
	v_readlane_b32 s4, v250, 6
	v_lshlrev_b64 v[22:23], 11, v[20:21]
	v_readlane_b32 s5, v250, 7
	v_pk_add_f32 v[18:19], v[18:19], v[54:55]
	v_pk_add_f32 v[16:17], v[16:17], v[52:53]
	v_lshl_add_u64 v[22:23], s[4:5], 0, v[22:23]
	v_lshl_add_u64 v[26:27], v[174:175], 1, v[22:23]
	v_pk_add_f32 v[14:15], v[14:15], v[46:47]
	v_pk_add_f32 v[12:13], v[12:13], v[44:45]
	v_pk_mul_f32 v[18:19], v[62:63], v[18:19]
	v_pk_mul_f32 v[16:17], v[60:61], v[16:17]
	v_pk_mul_f32 v[14:15], v[66:67], v[14:15]
	v_pk_mul_f32 v[12:13], v[64:65], v[12:13]
	v_pk_add_f32 v[10:11], v[10:11], v[42:43]
	v_pk_add_f32 v[8:9], v[8:9], v[40:41]
	v_pk_add_f32 v[4:5], v[4:5], v[36:37]
	v_pk_add_f32 v[6:7], v[6:7], v[38:39]
	v_pk_mul_f32 v[10:11], v[50:51], v[10:11]
	v_pk_mul_f32 v[8:9], v[48:49], v[8:9]
	v_pk_mul_f32 v[4:5], v[56:57], v[4:5]
	v_pk_mul_f32 v[6:7], v[58:59], v[6:7]
	s_waitcnt vmcnt(1)
	v_lshlrev_b32_e32 v28, 16, v224
	v_and_b32_e32 v22, 0xffff0000, v224
	v_lshlrev_b32_e32 v29, 16, v225
	v_and_b32_e32 v23, 0xffff0000, v225
	v_lshlrev_b32_e32 v31, 16, v227
	v_and_b32_e32 v25, 0xffff0000, v227
	v_lshlrev_b32_e32 v30, 16, v226
	v_and_b32_e32 v24, 0xffff0000, v226
	v_add_f32_e32 v16, v16, v28
	v_add_f32_e32 v17, v17, v22
	v_add_f32_e32 v18, v18, v29
	v_add_f32_e32 v19, v19, v23
	v_add_f32_e32 v15, v15, v25
	v_add_f32_e32 v22, v12, v30
	v_add_f32_e32 v23, v13, v24
	v_add_f32_e32 v24, v14, v31
	v_cvt_pk_bf16_f32 v12, v16, v17
	v_cvt_pk_bf16_f32 v13, v18, v19
	v_cvt_pk_bf16_f32 v14, v22, v23
	v_cvt_pk_bf16_f32 v15, v24, v15
	v_lshlrev_b32_e32 v22, 16, v12
	global_store_dwordx4 v[26:27], v[12:15], off
	v_lshlrev_b32_e32 v23, 16, v13
	v_lshlrev_b32_e32 v24, 16, v14
	v_and_b32_e32 v12, 0xffff0000, v12
	v_and_b32_e32 v13, 0xffff0000, v13
	v_and_b32_e32 v14, 0xffff0000, v14
	v_mul_f32_e32 v12, v12, v12
	v_mul_f32_e32 v13, v13, v13
	v_lshlrev_b32_e32 v25, 16, v15
	v_and_b32_e32 v15, 0xffff0000, v15
	v_mul_f32_e32 v14, v14, v14
	v_fmac_f32_e32 v12, v22, v22
	v_fmac_f32_e32 v13, v23, v23
	v_mul_f32_e32 v15, v15, v15
	v_fmac_f32_e32 v14, v24, v24
	v_add_f32_e32 v12, v12, v13
	v_fmac_f32_e32 v15, v25, v25
	v_add_f32_e32 v12, v12, v14
	v_add_f32_e32 v12, v12, v15
	s_waitcnt vmcnt(0)
	v_lshlrev_b32_e32 v13, 16, v228
	v_and_b32_e32 v14, 0xffff0000, v228
	v_lshlrev_b32_e32 v15, 16, v229
	v_and_b32_e32 v16, 0xffff0000, v229
	v_lshlrev_b32_e32 v17, 16, v230
	v_and_b32_e32 v18, 0xffff0000, v230
	v_lshlrev_b32_e32 v22, 16, v231
	v_and_b32_e32 v19, 0xffff0000, v231
	v_add_f32_e32 v8, v8, v13
	v_add_f32_e32 v11, v11, v16
	v_add_f32_e32 v5, v5, v18
	v_add_f32_e32 v9, v9, v14
	v_add_f32_e32 v10, v10, v15
	v_add_f32_e32 v4, v4, v17
	v_add_f32_e32 v13, v6, v22
	v_add_f32_e32 v14, v7, v19
	v_cvt_pk_bf16_f32 v6, v8, v9
	v_cvt_pk_bf16_f32 v7, v10, v11
	v_cvt_pk_bf16_f32 v8, v4, v5
	v_cvt_pk_bf16_f32 v9, v13, v14
	global_store_dwordx4 v[26:27], v[6:9], off offset:256
	v_and_b32_e32 v5, 0xffff0000, v6
	v_and_b32_e32 v11, 0xffff0000, v7
	v_lshlrev_b32_e32 v4, 16, v6
	v_lshlrev_b32_e32 v10, 16, v7
	v_and_b32_e32 v14, 0xffff0000, v8
	v_mul_f32_e32 v5, v5, v5
	v_mul_f32_e32 v11, v11, v11
	v_lshlrev_b32_e32 v13, 16, v8
	v_and_b32_e32 v16, 0xffff0000, v9
	v_mul_f32_e32 v14, v14, v14
	v_fmac_f32_e32 v5, v4, v4
	v_fmac_f32_e32 v11, v10, v10
	v_lshlrev_b32_e32 v15, 16, v9
	v_mul_f32_e32 v16, v16, v16
	v_fmac_f32_e32 v14, v13, v13
	v_add_f32_e32 v4, v5, v11
	v_add_f32_e32 v4, v4, v14
	v_fmac_f32_e32 v16, v15, v15
	v_add_f32_e32 v4, v4, v16
	v_add_f32_e32 v4, v12, v4
	ds_bpermute_b32 v5, v152, v4
	s_waitcnt lgkmcnt(0)
	v_add_f32_e32 v4, v4, v5
	ds_bpermute_b32 v5, v153, v4
	s_and_saveexec_b64 s[4:5], s[42:43]
	s_cbranch_execz .LBB0_1203
	v_readlane_b32 s24, v253, 54
	s_waitcnt lgkmcnt(0)
	v_add_f32_e32 v6, v4, v5
	s_lshl_b32 s20, s87, 2
	v_lshlrev_b64 v[4:5], 6, v[20:21]
	v_readlane_b32 s25, v253, 55
	s_ashr_i32 s21, s20, 31
	s_lshl_b32 s30, s82, 2
	v_lshl_add_u64 v[4:5], s[24:25], 0, v[4:5]
	v_lshl_add_u64 v[4:5], s[20:21], 2, v[4:5]
	v_lshl_add_u64 v[4:5], v[4:5], 0, s[30:31]
	global_store_dword v[4:5], v6, off
